# speedup vs baseline: 1.0153x; 1.0084x over previous
.Lk2f_b2:
	s_waitcnt lgkmcnt(0)
	s_barrier
	v_and_b32_e32 v1, 63, v0
	v_lshlrev_b32_e32 v6, 3, v1
	ds_read_b64 v[14:15], v6 offset:18688
	s_cmp_eq_u32 s4, 7
	s_cbranch_scc1 .Lk2f_w7
	s_waitcnt lgkmcnt(0)
	v_max_u32_e32 v8, v14, v15
	v_cmp_lt_u32_e32 vcc, 32, v8
	s_cmp_lg_u64 vcc, 0
	s_cbranch_scc1 .Lk2f_fallback
	v_add_u32_e32 v16, 3, v14
	v_add_u32_e32 v17, 3, v15
	s_movk_i32 s5, 49
	v_cmp_gt_u32_e32 vcc, s5, v1
	v_lshrrev_b32_e32 v16, 2, v16
	v_lshrrev_b32_e32 v17, 2, v17
	v_mov_b32_e32 v18, 0
	v_mov_b32_e32 v19, 0
	v_cndmask_b32_e32 v16, -1, v16, vcc
	v_cndmask_b32_e32 v17, -1, v17, vcc
	s_mov_b32 s6, 0
	v_cmp_eq_u32_e64 s[44:45], 8, v16
	v_cmp_eq_u32_e64 s[46:47], 8, v17
	s_bcnt1_i32_b64 s7, s[44:45]
	s_bcnt1_i32_b64 s38, s[46:47]
	v_mbcnt_lo_u32_b32 v20, s44, 0
	v_mbcnt_lo_u32_b32 v21, s46, 0
	v_mbcnt_hi_u32_b32 v20, s45, v20
	v_mbcnt_hi_u32_b32 v21, s47, v21
	v_add_u32_e32 v20, s6, v20
	s_add_i32 s6, s6, s7
	v_add_u32_e32 v21, s6, v21
	s_add_i32 s6, s6, s38
	v_cndmask_b32_e64 v18, v18, v20, s[44:45]
	v_cndmask_b32_e64 v19, v19, v21, s[46:47]
	v_cmp_eq_u32_e64 s[44:45], 7, v16
	v_cmp_eq_u32_e64 s[46:47], 7, v17
	s_bcnt1_i32_b64 s7, s[44:45]
	s_bcnt1_i32_b64 s38, s[46:47]
	v_mbcnt_lo_u32_b32 v20, s44, 0
	v_mbcnt_lo_u32_b32 v21, s46, 0
	v_mbcnt_hi_u32_b32 v20, s45, v20
	v_mbcnt_hi_u32_b32 v21, s47, v21
	v_add_u32_e32 v20, s6, v20
	s_add_i32 s6, s6, s7
	v_add_u32_e32 v21, s6, v21
	s_add_i32 s6, s6, s38
	v_cndmask_b32_e64 v18, v18, v20, s[44:45]
	v_cndmask_b32_e64 v19, v19, v21, s[46:47]
	v_cmp_eq_u32_e64 s[44:45], 6, v16
	v_cmp_eq_u32_e64 s[46:47], 6, v17
	s_bcnt1_i32_b64 s7, s[44:45]
	s_bcnt1_i32_b64 s38, s[46:47]
	v_mbcnt_lo_u32_b32 v20, s44, 0
	v_mbcnt_lo_u32_b32 v21, s46, 0
	v_mbcnt_hi_u32_b32 v20, s45, v20
	v_mbcnt_hi_u32_b32 v21, s47, v21
	v_add_u32_e32 v20, s6, v20
	s_add_i32 s6, s6, s7
	v_add_u32_e32 v21, s6, v21
	s_add_i32 s6, s6, s38
	v_cndmask_b32_e64 v18, v18, v20, s[44:45]
	v_cndmask_b32_e64 v19, v19, v21, s[46:47]
	v_cmp_eq_u32_e64 s[44:45], 5, v16
	v_cmp_eq_u32_e64 s[46:47], 5, v17
	s_bcnt1_i32_b64 s7, s[44:45]
	s_bcnt1_i32_b64 s38, s[46:47]
	v_mbcnt_lo_u32_b32 v20, s44, 0
	v_mbcnt_lo_u32_b32 v21, s46, 0
	v_mbcnt_hi_u32_b32 v20, s45, v20
	v_mbcnt_hi_u32_b32 v21, s47, v21
	v_add_u32_e32 v20, s6, v20
	s_add_i32 s6, s6, s7
	v_add_u32_e32 v21, s6, v21
	s_add_i32 s6, s6, s38
	v_cndmask_b32_e64 v18, v18, v20, s[44:45]
	v_cndmask_b32_e64 v19, v19, v21, s[46:47]
	v_cmp_eq_u32_e64 s[44:45], 4, v16
	v_cmp_eq_u32_e64 s[46:47], 4, v17
	s_bcnt1_i32_b64 s7, s[44:45]
	s_bcnt1_i32_b64 s38, s[46:47]
	v_mbcnt_lo_u32_b32 v20, s44, 0
	v_mbcnt_lo_u32_b32 v21, s46, 0
	v_mbcnt_hi_u32_b32 v20, s45, v20
	v_mbcnt_hi_u32_b32 v21, s47, v21
	v_add_u32_e32 v20, s6, v20
	s_add_i32 s6, s6, s7
	v_add_u32_e32 v21, s6, v21
	s_add_i32 s6, s6, s38
	v_cndmask_b32_e64 v18, v18, v20, s[44:45]
	v_cndmask_b32_e64 v19, v19, v21, s[46:47]
	v_cmp_eq_u32_e64 s[44:45], 3, v16
	v_cmp_eq_u32_e64 s[46:47], 3, v17
	s_bcnt1_i32_b64 s7, s[44:45]
	s_bcnt1_i32_b64 s38, s[46:47]
	v_mbcnt_lo_u32_b32 v20, s44, 0
	v_mbcnt_lo_u32_b32 v21, s46, 0
	v_mbcnt_hi_u32_b32 v20, s45, v20
	v_mbcnt_hi_u32_b32 v21, s47, v21
	v_add_u32_e32 v20, s6, v20
	s_add_i32 s6, s6, s7
	v_add_u32_e32 v21, s6, v21
	s_add_i32 s6, s6, s38
	v_cndmask_b32_e64 v18, v18, v20, s[44:45]
	v_cndmask_b32_e64 v19, v19, v21, s[46:47]
	v_cmp_eq_u32_e64 s[44:45], 2, v16
	v_cmp_eq_u32_e64 s[46:47], 2, v17
	s_bcnt1_i32_b64 s7, s[44:45]
	s_bcnt1_i32_b64 s38, s[46:47]
	v_mbcnt_lo_u32_b32 v20, s44, 0
	v_mbcnt_lo_u32_b32 v21, s46, 0
	v_mbcnt_hi_u32_b32 v20, s45, v20
	v_mbcnt_hi_u32_b32 v21, s47, v21
	v_add_u32_e32 v20, s6, v20
	s_add_i32 s6, s6, s7
	v_add_u32_e32 v21, s6, v21
	s_add_i32 s6, s6, s38
	v_cndmask_b32_e64 v18, v18, v20, s[44:45]
	v_cndmask_b32_e64 v19, v19, v21, s[46:47]
	v_cmp_eq_u32_e64 s[44:45], 1, v16
	v_cmp_eq_u32_e64 s[46:47], 1, v17
	s_bcnt1_i32_b64 s7, s[44:45]
	s_bcnt1_i32_b64 s38, s[46:47]
	v_mbcnt_lo_u32_b32 v20, s44, 0
	v_mbcnt_lo_u32_b32 v21, s46, 0
	v_mbcnt_hi_u32_b32 v20, s45, v20
	v_mbcnt_hi_u32_b32 v21, s47, v21
	v_add_u32_e32 v20, s6, v20
	s_add_i32 s6, s6, s7
	v_add_u32_e32 v21, s6, v21
	s_add_i32 s6, s6, s38
	v_cndmask_b32_e64 v18, v18, v20, s[44:45]
	v_cndmask_b32_e64 v19, v19, v21, s[46:47]
	v_cmp_eq_u32_e64 s[44:45], 0, v16
	v_cmp_eq_u32_e64 s[46:47], 0, v17
	s_bcnt1_i32_b64 s7, s[44:45]
	s_bcnt1_i32_b64 s38, s[46:47]
	v_mbcnt_lo_u32_b32 v20, s44, 0
	v_mbcnt_lo_u32_b32 v21, s46, 0
	v_mbcnt_hi_u32_b32 v20, s45, v20
	v_mbcnt_hi_u32_b32 v21, s47, v21
	v_add_u32_e32 v20, s6, v20
	s_add_i32 s6, s6, s7
	v_add_u32_e32 v21, s6, v21
	s_add_i32 s6, s6, s38
	v_cndmask_b32_e64 v18, v18, v20, s[44:45]
	v_cndmask_b32_e64 v19, v19, v21, s[46:47]
	v_lshlrev_b32_e32 v20, 1, v1
	v_lshlrev_b32_e32 v18, 2, v18
	v_lshlrev_b32_e32 v19, 2, v19
	v_or_b32_e32 v21, 1, v20
	v_lshl_or_b32 v20, v14, 8, v20
	v_lshl_or_b32 v21, v15, 8, v21
	s_and_saveexec_b64 s[38:39], vcc
	ds_write_b32 v18, v20 offset:33712
	ds_write_b32 v19, v21 offset:33712
	s_mov_b64 exec, s[38:39]
	s_lshl_b32 s5, s4, 4
	v_lshrrev_b32_e32 v3, 2, v1
	v_add_u32_e32 v6, s5, v3
	v_and_b32_e32 v8, 15, v0
	v_add_u32_e32 v9, s5, v8
	v_min_u32_e32 v7, 0x61, v6
	v_min_u32_e32 v10, 0x61, v9
	v_lshlrev_b32_e32 v7, 2, v7
	v_lshlrev_b32_e32 v10, 2, v10
	ds_read_b32 v7, v7 offset:33712
	ds_read_b32 v10, v10 offset:33712
	s_movk_i32 s7, 0x62
	v_cmp_gt_u32_e32 vcc, s7, v6
	v_cmp_gt_u32_e64 s[38:39], s7, v9
	v_mov_b32_e32 v8, 0x62
	v_and_b32_e32 v11, 3, v1
	v_lshlrev_b32_e32 v1, 4, v11
	s_mov_b32 s32, s8
	s_and_b32 s33, s9, 0xffff
	s_mov_b32 s34, 0xc35000
	s_mov_b32 s35, 0x20000
	s_waitcnt lgkmcnt(0)
	v_and_b32_e32 v12, 0xff, v7
	v_lshrrev_b32_e32 v3, 8, v7
	v_cndmask_b32_e32 v12, v8, v12, vcc
	v_cndmask_b32_e32 v3, 0, v3, vcc
	v_mul_u32_u24_e32 v2, 0x90, v12
	ds_read_b128 v[4:7], v2 offset:19456
	v_and_b32_e32 v10, 0xff, v10
	s_mul_i32 s6, s3, 0x62
	v_add_u32_e32 v9, s6, v10
	s_mov_b32 s7, 0x186a0
	v_cmp_gt_u32_e32 vcc, s7, v9
	s_and_b64 vcc, vcc, s[38:39]
	s_mov_b64 s[40:41], vcc
	v_and_b32_e32 v8, 0x30, v0
	v_cndmask_b32_e32 v9, 0, v9, vcc
	v_lshl_or_b32 v8, v9, 7, v8
	buffer_load_dwordx4 v[56:59], v8, s[32:35], 0 offen
	buffer_load_dwordx4 v[60:63], v8, s[32:35], 0 offen offset:64
	v_mov_b32_e32 v40, 0
	v_mov_b32_e32 v41, 0
	v_mov_b32_e32 v42, 0
	v_mov_b32_e32 v43, 0
	v_mov_b32_e32 v44, 0
	v_mov_b32_e32 v45, 0
	v_mov_b32_e32 v46, 0
	v_mov_b32_e32 v47, 0
	v_mov_b32_e32 v48, 0
	v_mov_b32_e32 v49, 0
	v_mov_b32_e32 v50, 0
	v_mov_b32_e32 v51, 0
	v_mov_b32_e32 v52, 0
	v_mov_b32_e32 v53, 0
	v_mov_b32_e32 v54, 0
	v_mov_b32_e32 v55, 0
	s_mov_b32 s5, 0
	v_cmp_lt_i32_e32 vcc, 0, v3
	s_waitcnt lgkmcnt(0)
	s_cmp_lg_u64 vcc, 0
	s_cbranch_scc0 .Lk2f_gdone

.Lk2f_gdone:
	v_and_b32_e32 v2, 63, v0
	v_lshrrev_b32_e32 v5, 4, v2
	v_lshlrev_b32_e32 v7, 4, v5
	v_lshlrev_b32_e32 v6, 4, v2
	ds_read_b128 v[24:27], v7 offset:18432
	ds_read_b128 v[28:31], v7 offset:18496
	ds_read_b128 v[32:35], v7 offset:18560
	ds_read_b128 v[36:39], v7 offset:18624
	v_and_b32_e32 v16, 15, v2
	v_lshl_or_b32 v5, v16, 2, v5
	v_lshlrev_b32_e32 v5, 2, v5
	v_cvt_f32_i32_e32 v4, v3
	s_lshl_b32 s5, s4, 4
	v_add_u32_e32 v3, s5, v16
	v_min_u32_e32 v3, 0x61, v3
	v_lshlrev_b32_e32 v3, 2, v3
	ds_read_b32 v3, v3 offset:33712
	v_max_f32_e32 v4, 1.0, v4
	v_div_scale_f32 v16, s[6:7], v4, v4, 1.0
	v_rcp_f32_e32 v17, v16
	s_nop 0
	v_fma_f32 v18, -v16, v17, 1.0
	v_fmac_f32_e32 v17, v18, v17
	v_div_scale_f32 v18, vcc, 1.0, v4, 1.0
	v_mul_f32_e32 v19, v18, v17
	v_fma_f32 v8, -v16, v19, v18
	v_fmac_f32_e32 v19, v8, v17
	v_fma_f32 v16, -v16, v19, v18
	v_div_fmas_f32 v16, v16, v17, v19
	v_div_fixup_f32 v4, v16, v4, 1.0
	v_mul_f32_e32 v40, v4, v40
	v_mul_f32_e32 v41, v4, v41
	v_mul_f32_e32 v42, v4, v42
	v_mul_f32_e32 v43, v4, v43
	v_mul_f32_e32 v44, v4, v44
	v_mul_f32_e32 v45, v4, v45
	v_mul_f32_e32 v46, v4, v46
	v_mul_f32_e32 v47, v4, v47
	v_mul_f32_e32 v48, v4, v48
	v_mul_f32_e32 v49, v4, v49
	v_mul_f32_e32 v50, v4, v50
	v_mul_f32_e32 v51, v4, v51
	v_mul_f32_e32 v52, v4, v52
	v_mul_f32_e32 v53, v4, v53
	v_mul_f32_e32 v54, v4, v54
	v_mul_f32_e32 v55, v4, v55
	v_cvt_pk_f16_f32 v8, v40, v41
	v_cvt_pk_f16_f32 v9, v42, v43
	v_cvt_pk_f16_f32 v10, v44, v45
	v_cvt_pk_f16_f32 v11, v46, v47
	v_cvt_pk_f16_f32 v12, v48, v49
	v_cvt_pk_f16_f32 v13, v50, v51
	v_cvt_pk_f16_f32 v14, v52, v53
	v_cvt_pk_f16_f32 v15, v54, v55
	s_waitcnt lgkmcnt(0)
	ds_bpermute_b32 v16, v5, v8
	ds_bpermute_b32 v17, v5, v9
	ds_bpermute_b32 v18, v5, v10
	ds_bpermute_b32 v19, v5, v11
	ds_bpermute_b32 v20, v5, v12
	ds_bpermute_b32 v21, v5, v13
	ds_bpermute_b32 v22, v5, v14
	ds_bpermute_b32 v23, v5, v15
	ds_read_b128 v[40:43], v6 offset:0
	ds_read_b128 v[44:47], v6 offset:1024
	ds_read_b128 v[48:51], v6 offset:2048
	ds_read_b128 v[52:55], v6 offset:3072
	s_waitcnt vmcnt(0)
	s_waitcnt lgkmcnt(3)
	v_mfma_f32_16x16x32_f16 v[24:27], v[40:43], v[16:19], v[24:27]
	s_waitcnt lgkmcnt(2)
	v_mfma_f32_16x16x32_f16 v[24:27], v[44:47], v[20:23], v[24:27]
	s_waitcnt lgkmcnt(1)
	v_mfma_f32_16x16x32_f16 v[24:27], v[48:51], v[56:59], v[24:27]
	s_waitcnt lgkmcnt(0)
	v_mfma_f32_16x16x32_f16 v[24:27], v[52:55], v[60:63], v[24:27]
	ds_read_b128 v[40:43], v6 offset:4096
	ds_read_b128 v[44:47], v6 offset:5120
	ds_read_b128 v[48:51], v6 offset:6144
	ds_read_b128 v[52:55], v6 offset:7168
	s_waitcnt lgkmcnt(3)
	v_mfma_f32_16x16x32_f16 v[28:31], v[40:43], v[16:19], v[28:31]
	s_waitcnt lgkmcnt(2)
	v_mfma_f32_16x16x32_f16 v[28:31], v[44:47], v[20:23], v[28:31]
	s_waitcnt lgkmcnt(1)
	v_mfma_f32_16x16x32_f16 v[28:31], v[48:51], v[56:59], v[28:31]
	s_waitcnt lgkmcnt(0)
	v_mfma_f32_16x16x32_f16 v[28:31], v[52:55], v[60:63], v[28:31]
	ds_read_b128 v[40:43], v6 offset:8192
	ds_read_b128 v[44:47], v6 offset:9216
	ds_read_b128 v[48:51], v6 offset:10240
	ds_read_b128 v[52:55], v6 offset:11264
	s_waitcnt lgkmcnt(3)
	v_mfma_f32_16x16x32_f16 v[32:35], v[40:43], v[16:19], v[32:35]
	s_waitcnt lgkmcnt(2)
	v_mfma_f32_16x16x32_f16 v[32:35], v[44:47], v[20:23], v[32:35]
	s_waitcnt lgkmcnt(1)
	v_mfma_f32_16x16x32_f16 v[32:35], v[48:51], v[56:59], v[32:35]
	s_waitcnt lgkmcnt(0)
	v_mfma_f32_16x16x32_f16 v[32:35], v[52:55], v[60:63], v[32:35]
	ds_read_b128 v[40:43], v6 offset:12288
	ds_read_b128 v[44:47], v6 offset:13312
	ds_read_b128 v[48:51], v6 offset:14336
	ds_read_b128 v[52:55], v6 offset:15360
	s_waitcnt lgkmcnt(3)
	v_mfma_f32_16x16x32_f16 v[36:39], v[40:43], v[16:19], v[36:39]
	s_waitcnt lgkmcnt(2)
	v_mfma_f32_16x16x32_f16 v[36:39], v[44:47], v[20:23], v[36:39]
	s_waitcnt lgkmcnt(1)
	v_mfma_f32_16x16x32_f16 v[36:39], v[48:51], v[56:59], v[36:39]
	s_waitcnt lgkmcnt(0)
	v_mfma_f32_16x16x32_f16 v[36:39], v[52:55], v[60:63], v[36:39]
	ds_read_b128 v[40:43], v6 offset:16384
	ds_read_b128 v[44:47], v6 offset:17408
	v_max_f32_e32 v24, 0, v24
	v_max_f32_e32 v25, 0, v25
	v_max_f32_e32 v26, 0, v26
	v_max_f32_e32 v27, 0, v27
	v_cvt_pk_f16_f32 v8, v24, v25
	v_cvt_pk_f16_f32 v9, v26, v27
	v_max_f32_e32 v28, 0, v28
	v_max_f32_e32 v29, 0, v29
	v_max_f32_e32 v30, 0, v30
	v_max_f32_e32 v31, 0, v31
	v_cvt_pk_f16_f32 v10, v28, v29
	v_cvt_pk_f16_f32 v11, v30, v31
	v_max_f32_e32 v32, 0, v32
	v_max_f32_e32 v33, 0, v33
	v_max_f32_e32 v34, 0, v34
	v_max_f32_e32 v35, 0, v35
	v_cvt_pk_f16_f32 v12, v32, v33
	v_cvt_pk_f16_f32 v13, v34, v35
	v_max_f32_e32 v36, 0, v36
	v_max_f32_e32 v37, 0, v37
	v_max_f32_e32 v38, 0, v38
	v_max_f32_e32 v39, 0, v39
	v_cvt_pk_f16_f32 v14, v36, v37
	v_cvt_pk_f16_f32 v15, v38, v39
	v_mov_b32_e32 v4, 0
	v_mov_b32_e32 v5, 0
	v_mov_b32_e32 v6, s36
	v_mov_b32_e32 v7, s37
	s_waitcnt lgkmcnt(0)
	s_nop 1
	v_mfma_f32_16x16x32_f16 v[4:7], v[40:43], v[8:11], v[4:7]
	v_mfma_f32_16x16x32_f16 v[4:7], v[44:47], v[12:15], v[4:7]
	s_mul_i32 s6, s3, 0x62
	v_and_b32_e32 v8, 0xff, v3
	v_add_u32_e32 v8, s6, v8
	v_lshlrev_b32_e32 v8, 3, v8
	v_cmp_gt_u32_e32 vcc, 16, v2
	s_and_b64 vcc, vcc, s[40:41]
	s_and_saveexec_b64 s[6:7], vcc
	s_cbranch_execz .Lk2f_exit
	s_nop 7
	global_store_dwordx2 v8, v[4:5], s[26:27]
	global_store_dwordx2 v8, v[6:7], s[28:29]
	s_endpgm

	.amdhsa_kernel _Z8k_layer1PKDF16_PKiS2_PiS3_PKDv4_jS6_PKfS8_P15HIP_vector_typeIfLj2EESB_
		.amdhsa_group_segment_fixed_size 34224
		.amdhsa_private_segment_fixed_size 0
		.amdhsa_kernarg_size 88
		.amdhsa_user_sgpr_count 2
		.amdhsa_user_sgpr_dispatch_ptr 0
		.amdhsa_user_sgpr_queue_ptr 0
		.amdhsa_user_sgpr_kernarg_segment_ptr 1
		.amdhsa_user_sgpr_dispatch_id 0
		.amdhsa_user_sgpr_kernarg_preload_length 0
		.amdhsa_user_sgpr_kernarg_preload_offset 0
		.amdhsa_user_sgpr_private_segment_size 0
		.amdhsa_uses_dynamic_stack 0
		.amdhsa_enable_private_segment 0
		.amdhsa_system_sgpr_workgroup_id_x 1
		.amdhsa_system_sgpr_workgroup_id_y 0
		.amdhsa_system_sgpr_workgroup_id_z 0
		.amdhsa_system_sgpr_workgroup_info 0
		.amdhsa_system_vgpr_workitem_id 0
		.amdhsa_next_free_vgpr 64
		.amdhsa_next_free_sgpr 70
		.amdhsa_accum_offset 64
		.amdhsa_reserve_vcc 1
		.amdhsa_float_round_mode_32 0
		.amdhsa_float_round_mode_16_64 0
		.amdhsa_float_denorm_mode_32 3
		.amdhsa_float_denorm_mode_16_64 3
		.amdhsa_dx10_clamp 1
		.amdhsa_ieee_mode 1
		.amdhsa_fp16_overflow 0
		.amdhsa_tg_split 0
		.amdhsa_exception_fp_ieee_invalid_op 0
		.amdhsa_exception_fp_denorm_src 0
		.amdhsa_exception_fp_ieee_div_zero 0
		.amdhsa_exception_fp_ieee_overflow 0
		.amdhsa_exception_fp_ieee_underflow 0
		.amdhsa_exception_fp_ieee_inexact 0
		.amdhsa_exception_int_div_zero 0
	.end_amdhsa_kernel

amdhsa.kernels:
  - .agpr_count:     0
    .args:
      - .actual_access:  read_only
        .address_space:  global
        .offset:         0
        .size:           8
        .value_kind:     global_buffer
      - .actual_access:  read_only
        .address_space:  global
        .offset:         8
        .size:           8
        .value_kind:     global_buffer
      - .actual_access:  read_only
        .address_space:  global
        .offset:         16
        .size:           8
        .value_kind:     global_buffer
      - .actual_access:  read_only
        .address_space:  global
        .offset:         24
        .size:           8
        .value_kind:     global_buffer
      - .actual_access:  read_only
        .address_space:  global
        .offset:         32
        .size:           8
        .value_kind:     global_buffer
      - .actual_access:  read_only
        .address_space:  global
        .offset:         40
        .size:           8
        .value_kind:     global_buffer
      - .actual_access:  write_only
        .address_space:  global
        .offset:         48
        .size:           8
        .value_kind:     global_buffer
      - .actual_access:  write_only
        .address_space:  global
        .offset:         56
        .size:           8
        .value_kind:     global_buffer
      - .actual_access:  write_only
        .address_space:  global
        .offset:         64
        .size:           8
        .value_kind:     global_buffer
      - .actual_access:  write_only
        .address_space:  global
        .offset:         72
        .size:           8
        .value_kind:     global_buffer
      - .actual_access:  write_only
        .address_space:  global
        .offset:         80
        .size:           8
        .value_kind:     global_buffer
    .group_segment_fixed_size: 20544
    .kernarg_segment_align: 8
    .kernarg_segment_size: 88
    .language:       OpenCL C
    .language_version:
      - 2
      - 0
    .max_flat_workgroup_size: 1024
    .name:           _Z6k_partPKiPKfS2_S2_S2_S2_PiS3_PDF16_S4_S4_
    .private_segment_fixed_size: 0
    .sgpr_count:     28
    .sgpr_spill_count: 0
    .symbol:         _Z6k_partPKiPKfS2_S2_S2_S2_PiS3_PDF16_S4_S4_.kd
    .uniform_work_group_size: 1
    .uses_dynamic_stack: false
    .vgpr_count:     44
    .vgpr_spill_count: 0
    .wavefront_size: 64
  - .agpr_count:     0
    .args:
      - .actual_access:  read_only
        .address_space:  global
        .offset:         0
        .size:           8
        .value_kind:     global_buffer
      - .actual_access:  read_only
        .address_space:  global
        .offset:         8
        .size:           8
        .value_kind:     global_buffer
      - .actual_access:  read_only
        .address_space:  global
        .offset:         16
        .size:           8
        .value_kind:     global_buffer
      - .actual_access:  write_only
        .address_space:  global
        .offset:         24
        .size:           8
        .value_kind:     global_buffer
      - .address_space:  global
        .offset:         32
        .size:           8
        .value_kind:     global_buffer
      - .actual_access:  read_only
        .address_space:  global
        .offset:         40
        .size:           8
        .value_kind:     global_buffer
      - .actual_access:  read_only
        .address_space:  global
        .offset:         48
        .size:           8
        .value_kind:     global_buffer
      - .actual_access:  read_only
        .address_space:  global
        .offset:         56
        .size:           8
        .value_kind:     global_buffer
      - .actual_access:  read_only
        .address_space:  global
        .offset:         64
        .size:           8
        .value_kind:     global_buffer
      - .actual_access:  write_only
        .address_space:  global
        .offset:         72
        .size:           8
        .value_kind:     global_buffer
      - .actual_access:  write_only
        .address_space:  global
        .offset:         80
        .size:           8
        .value_kind:     global_buffer
    .group_segment_fixed_size: 34224
    .kernarg_segment_align: 8
    .kernarg_segment_size: 88
    .language:       OpenCL C
    .language_version:
      - 2
      - 0
    .max_flat_workgroup_size: 512
    .name:           _Z8k_layer1PKDF16_PKiS2_PiS3_PKDv4_jS6_PKfS8_P15HIP_vector_typeIfLj2EESB_
    .private_segment_fixed_size: 0
    .sgpr_count:     76
    .sgpr_spill_count: 0
    .symbol:         _Z8k_layer1PKDF16_PKiS2_PiS3_PKDv4_jS6_PKfS8_P15HIP_vector_typeIfLj2EESB_.kd
    .uniform_work_group_size: 1
    .uses_dynamic_stack: false
    .vgpr_count:     64
    .vgpr_spill_count: 0
    .wavefront_size: 64
  - .agpr_count:     0
    .args:
      - .actual_access:  read_only
        .address_space:  global
        .offset:         0
        .size:           8
        .value_kind:     global_buffer
      - .actual_access:  read_only
        .address_space:  global
        .offset:         8
        .size:           8
        .value_kind:     global_buffer
      - .actual_access:  read_only
        .address_space:  global
        .offset:         16
        .size:           8
        .value_kind:     global_buffer
      - .actual_access:  read_only
        .address_space:  global
        .offset:         24
        .size:           8
        .value_kind:     global_buffer
      - .actual_access:  write_only
        .address_space:  global
        .offset:         32
        .size:           8
        .value_kind:     global_buffer
    .group_segment_fixed_size: 0
    .kernarg_segment_align: 8
    .kernarg_segment_size: 40
    .language:       OpenCL C
    .language_version:
      - 2
      - 0
    .max_flat_workgroup_size: 448
    .name:           _Z8k_layer2PK15HIP_vector_typeIfLj2EES2_PKiS4_PS0_
    .private_segment_fixed_size: 0
    .sgpr_count:     21
    .sgpr_spill_count: 0
    .symbol:         _Z8k_layer2PK15HIP_vector_typeIfLj2EES2_PKiS4_PS0_.kd
    .uniform_work_group_size: 1
    .uses_dynamic_stack: false
    .vgpr_count:     25
    .vgpr_spill_count: 0
    .wavefront_size: 64
